# combined: snake MFMA order + non-leader workgroups poll the top barrier generation directly + leading half starts SwiGLU epilogue before the align barrier (removed 2x s_nop 15 pad)
# speedup vs baseline: 1.0076x; 1.0069x over previous
.LBB0_90:
	s_lshl_b32 s3, s2, 8
	s_add_u32 s6, s16, s3
	s_addc_u32 s7, s17, 0
	v_mov_b32_e32 v2, 0x1000
	v_mov_b32_e32 v4, 1
	global_atomic_add v4, v2, v4, s[6:7] offset:1024 sc0
	v_cvt_f32_u32_e32 v2, v3
	v_sub_u32_e32 v5, 0, v3
	v_rcp_iflag_f32_e32 v2, v2
	s_nop 0
	v_mul_f32_e32 v2, 0x4f7ffffe, v2
	v_cvt_u32_f32_e32 v2, v2
	v_mul_lo_u32 v5, v5, v2
	v_mul_hi_u32 v5, v2, v5
	v_add_u32_e32 v2, v2, v5
	s_waitcnt vmcnt(0)
	v_mul_hi_u32 v2, v4, v2
	v_mul_lo_u32 v5, v2, v3
	v_sub_u32_e32 v5, v4, v5
	v_add_u32_e32 v6, 1, v2
	v_cmp_ge_u32_e32 vcc, v5, v3
	v_add_u32_e32 v4, 1, v4
	s_nop 0
	v_cndmask_b32_e32 v2, v2, v6, vcc
	v_sub_u32_e32 v6, v5, v3
	v_cndmask_b32_e32 v5, v5, v6, vcc
	v_add_u32_e32 v6, 1, v2
	v_cmp_ge_u32_e32 vcc, v5, v3
	s_nop 1
	v_cndmask_b32_e32 v2, v2, v6, vcc
	v_mul_lo_u32 v5, v3, v2
	v_add_u32_e32 v3, v5, v3
	v_cmp_ne_u32_e32 vcc, v4, v3
	s_and_saveexec_b64 s[8:9], vcc
	s_xor_b64 s[8:9], exec, s[8:9]
	s_cbranch_execz .LBB0_104
	s_waitcnt lgkmcnt(0)
	s_add_u32 s20, s82, 0x7500
	s_addc_u32 s21, s83, 0
	v_mov_b32_e32 v1, 0
	s_nop 1
	global_load_dword v1, v1, s[20:21] sc1
	s_waitcnt vmcnt(0)
	v_cmp_eq_u32_e32 vcc, v1, v2
	s_and_saveexec_b64 s[10:11], vcc
	s_cbranch_execz .LBB0_103
	s_add_u32 s18, s82, 0x4200
	s_addc_u32 s19, s83, 0
	s_mov_b32 s3, 1
	s_mov_b64 s[22:23], 0
	v_mov_b32_e32 v1, 0
	s_branch .LBB0_94

.LBB0_192:
	v_readlane_b32 s8, v252, 62
	v_readlane_b32 s9, v252, 63
	v_cvt_f32_u32_e32 v3, v4
	v_sub_u32_e32 v6, 0, v4
	v_rcp_iflag_f32_e32 v3, v3
	s_nop 1
	global_atomic_add v5, v35, v246, s[8:9] sc0
	v_mul_f32_e32 v3, 0x4f7ffffe, v3
	v_cvt_u32_f32_e32 v3, v3
	v_mul_lo_u32 v6, v6, v3
	v_mul_hi_u32 v6, v3, v6
	v_add_u32_e32 v3, v3, v6
	s_waitcnt vmcnt(0)
	v_mul_hi_u32 v3, v5, v3
	v_mul_lo_u32 v6, v3, v4
	v_sub_u32_e32 v6, v5, v6
	v_add_u32_e32 v7, 1, v3
	v_cmp_ge_u32_e32 vcc, v6, v4
	v_add_u32_e32 v5, 1, v5
	s_nop 0
	v_cndmask_b32_e32 v3, v3, v7, vcc
	v_sub_u32_e32 v7, v6, v4
	v_cndmask_b32_e32 v6, v6, v7, vcc
	v_add_u32_e32 v7, 1, v3
	v_cmp_ge_u32_e32 vcc, v6, v4
	s_nop 1
	v_cndmask_b32_e32 v3, v3, v7, vcc
	v_mul_lo_u32 v6, v4, v3
	v_add_u32_e32 v4, v6, v4
	v_cmp_ne_u32_e32 vcc, v5, v4
	s_and_saveexec_b64 s[8:9], vcc
	s_xor_b64 s[8:9], exec, s[8:9]
	s_cbranch_execz .LBB0_221
	s_waitcnt lgkmcnt(0)
	v_readlane_b32 s98, v254, 57
	v_readlane_b32 s99, v254, 58
	s_nop 0
	s_add_u32 s98, s98, 0x3300
	s_addc_u32 s99, s99, 0
	s_nop 1
	global_load_dword v2, v35, s[98:99] sc1
	s_waitcnt vmcnt(0)
	v_cmp_eq_u32_e32 vcc, v2, v3
	s_and_saveexec_b64 s[10:11], vcc
	s_cbranch_execz .LBB0_220
	s_mov_b32 s15, 1
	s_mov_b64 s[16:17], 0
	s_branch .LBB0_196

.LBB0_198:
	global_load_dword v2, v35, s[98:99] sc1
	s_add_i32 s15, s15, 1
	s_mov_b64 s[36:37], -1
	s_waitcnt vmcnt(0)
	v_cmp_ne_u32_e32 vcc, v2, v3
	s_orn2_b64 s[30:31], vcc, exec
	s_branch .LBB0_195

.LBB0_207:
	v_readlane_b32 s6, v252, 62
	v_readlane_b32 s7, v252, 63
	v_cvt_f32_u32_e32 v1, v3
	v_sub_u32_e32 v5, 0, v3
	v_rcp_iflag_f32_e32 v1, v1
	s_nop 1
	global_atomic_add v4, v35, v246, s[6:7] sc0
	v_mul_f32_e32 v1, 0x4f7ffffe, v1
	v_cvt_u32_f32_e32 v1, v1
	v_mul_lo_u32 v5, v5, v1
	v_mul_hi_u32 v5, v1, v5
	v_add_u32_e32 v1, v1, v5
	s_waitcnt vmcnt(0)
	v_mul_hi_u32 v1, v4, v1
	v_mul_lo_u32 v5, v1, v3
	v_sub_u32_e32 v5, v4, v5
	v_add_u32_e32 v6, 1, v1
	v_cmp_ge_u32_e32 vcc, v5, v3
	v_add_u32_e32 v4, 1, v4
	s_nop 0
	v_cndmask_b32_e32 v1, v1, v6, vcc
	v_sub_u32_e32 v6, v5, v3
	v_cndmask_b32_e32 v5, v5, v6, vcc
	v_add_u32_e32 v6, 1, v1
	v_cmp_ge_u32_e32 vcc, v5, v3
	s_nop 1
	v_cndmask_b32_e32 v1, v1, v6, vcc
	v_mul_lo_u32 v5, v3, v1
	v_add_u32_e32 v3, v5, v3
	v_cmp_ne_u32_e32 vcc, v4, v3
	s_and_saveexec_b64 s[6:7], vcc
	s_xor_b64 s[6:7], exec, s[6:7]
	s_cbranch_execz .LBB0_238
	s_waitcnt lgkmcnt(0)
	v_readlane_b32 s98, v254, 57
	v_readlane_b32 s99, v254, 58
	s_nop 0
	s_add_u32 s98, s98, 0x3300
	s_addc_u32 s99, s99, 0
	s_nop 1
	global_load_dword v2, v35, s[98:99] sc1
	s_waitcnt vmcnt(0)
	v_cmp_eq_u32_e32 vcc, v2, v1
	s_and_saveexec_b64 s[8:9], vcc
	s_cbranch_execz .LBB0_237
	s_mov_b32 s15, 1
	s_mov_b64 s[10:11], 0
	s_branch .LBB0_211

.LBB0_213:
	global_load_dword v2, v35, s[98:99] sc1
	s_add_i32 s15, s15, 1
	s_mov_b64 s[30:31], -1
	s_waitcnt vmcnt(0)
	v_cmp_ne_u32_e32 vcc, v2, v1
	s_orn2_b64 s[22:23], vcc, exec
	s_branch .LBB0_210

.LBB0_256:
	v_readlane_b32 s10, v252, 62
	v_readlane_b32 s11, v252, 63
	v_cvt_f32_u32_e32 v3, v4
	v_sub_u32_e32 v6, 0, v4
	v_rcp_iflag_f32_e32 v3, v3
	s_nop 1
	global_atomic_add v5, v35, v246, s[10:11] sc0
	v_mul_f32_e32 v3, 0x4f7ffffe, v3
	v_cvt_u32_f32_e32 v3, v3
	v_mul_lo_u32 v6, v6, v3
	v_mul_hi_u32 v6, v3, v6
	v_add_u32_e32 v3, v3, v6
	s_waitcnt vmcnt(0)
	v_mul_hi_u32 v3, v5, v3
	v_mul_lo_u32 v6, v3, v4
	v_sub_u32_e32 v6, v5, v6
	v_add_u32_e32 v7, 1, v3
	v_cmp_ge_u32_e32 vcc, v6, v4
	v_add_u32_e32 v5, 1, v5
	s_nop 0
	v_cndmask_b32_e32 v3, v3, v7, vcc
	v_sub_u32_e32 v7, v6, v4
	v_cndmask_b32_e32 v6, v6, v7, vcc
	v_add_u32_e32 v7, 1, v3
	v_cmp_ge_u32_e32 vcc, v6, v4
	s_nop 1
	v_cndmask_b32_e32 v3, v3, v7, vcc
	v_mul_lo_u32 v6, v4, v3
	v_add_u32_e32 v4, v6, v4
	v_cmp_ne_u32_e32 vcc, v5, v4
	s_and_saveexec_b64 s[10:11], vcc
	s_xor_b64 s[10:11], exec, s[10:11]
	s_cbranch_execz .LBB0_694
	s_waitcnt lgkmcnt(0)
	v_readlane_b32 s98, v254, 57
	v_readlane_b32 s99, v254, 58
	s_nop 0
	s_add_u32 s98, s98, 0x3300
	s_addc_u32 s99, s99, 0
	s_nop 1
	global_load_dword v2, v35, s[98:99] sc1
	s_waitcnt vmcnt(0)
	v_cmp_eq_u32_e32 vcc, v2, v3
	s_and_saveexec_b64 s[30:31], vcc
	s_cbranch_execz .LBB0_693
	s_mov_b32 s15, 1
	s_mov_b64 s[36:37], 0
	s_branch .LBB0_260

.LBB0_262:
	global_load_dword v2, v35, s[98:99] sc1
	s_add_i32 s15, s15, 1
	s_mov_b64 s[44:45], -1
	s_waitcnt vmcnt(0)
	v_cmp_ne_u32_e32 vcc, v2, v3
	s_orn2_b64 s[42:43], vcc, exec
	s_branch .LBB0_259

.LBB0_311:
	v_readlane_b32 s6, v252, 62
	v_readlane_b32 s7, v252, 63
	v_cvt_f32_u32_e32 v1, v3
	v_sub_u32_e32 v5, 0, v3
	v_rcp_iflag_f32_e32 v1, v1
	s_nop 1
	global_atomic_add v4, v35, v246, s[6:7] sc0
	v_mul_f32_e32 v1, 0x4f7ffffe, v1
	v_cvt_u32_f32_e32 v1, v1
	v_mul_lo_u32 v5, v5, v1
	v_mul_hi_u32 v5, v1, v5
	v_add_u32_e32 v1, v1, v5
	s_waitcnt vmcnt(0)
	v_mul_hi_u32 v1, v4, v1
	v_mul_lo_u32 v5, v1, v3
	v_sub_u32_e32 v5, v4, v5
	v_add_u32_e32 v6, 1, v1
	v_cmp_ge_u32_e32 vcc, v5, v3
	v_add_u32_e32 v4, 1, v4
	s_nop 0
	v_cndmask_b32_e32 v1, v1, v6, vcc
	v_sub_u32_e32 v6, v5, v3
	v_cndmask_b32_e32 v5, v5, v6, vcc
	v_add_u32_e32 v6, 1, v1
	v_cmp_ge_u32_e32 vcc, v5, v3
	s_nop 1
	v_cndmask_b32_e32 v1, v1, v6, vcc
	v_mul_lo_u32 v5, v3, v1
	v_add_u32_e32 v3, v5, v3
	v_cmp_ne_u32_e32 vcc, v4, v3
	s_and_saveexec_b64 s[6:7], vcc
	s_xor_b64 s[6:7], exec, s[6:7]
	s_cbranch_execz .LBB0_325
	s_waitcnt lgkmcnt(0)
	v_readlane_b32 s98, v254, 57
	v_readlane_b32 s99, v254, 58
	s_nop 0
	s_add_u32 s98, s98, 0x3300
	s_addc_u32 s99, s99, 0
	s_nop 1
	global_load_dword v2, v35, s[98:99] sc1
	s_waitcnt vmcnt(0)
	v_cmp_eq_u32_e32 vcc, v2, v1
	s_and_saveexec_b64 s[8:9], vcc
	s_cbranch_execz .LBB0_324
	s_mov_b32 s26, 1
	s_mov_b64 s[10:11], 0
	s_branch .LBB0_315

.LBB0_317:
	global_load_dword v2, v35, s[98:99] sc1
	s_add_i32 s26, s26, 1
	s_mov_b64 s[30:31], -1
	s_waitcnt vmcnt(0)
	v_cmp_ne_u32_e32 vcc, v2, v1
	s_orn2_b64 s[22:23], vcc, exec
	s_branch .LBB0_314

.LBB0_823:
.LBB0_825:
	v_exp_f32_e64 v18, -v156
	v_exp_f32_e64 v19, -v157
	v_pk_mul_f32 v[16:17], v[156:157], v[124:125]
	v_pk_mul_f32 v[10:11], v[162:163], v[130:131]
	v_exp_f32_e64 v14, -v160
	v_pk_add_f32 v[18:19], v[18:19], 1.0 op_sel_hi:[1,0]
	v_exp_f32_e64 v15, -v161
	v_rcp_f32_e32 v18, v18
	v_rcp_f32_e32 v19, v19
	v_pk_mul_f32 v[12:13], v[160:161], v[128:129]
	v_pk_add_f32 v[14:15], v[14:15], 1.0 op_sel_hi:[1,0]
	s_add_u32 s8, s81, 0xfffffe00
	v_pk_mul_f32 v[16:17], v[18:19], v[16:17]
	v_exp_f32_e64 v18, -v162
	v_exp_f32_e64 v19, -v163
	v_rcp_f32_e32 v14, v14
	v_rcp_f32_e32 v15, v15
	s_addc_u32 s9, s82, -1
	v_pk_add_f32 v[18:19], v[18:19], 1.0 op_sel_hi:[1,0]
	v_mov_b32_e32 v3, v1
	v_rcp_f32_e32 v18, v18
	v_rcp_f32_e32 v19, v19
	v_pk_mul_f32 v[12:13], v[14:15], v[12:13]
	v_pk_mul_f32 v[14:15], v[158:159], v[126:127]
	v_med3_f32 v7, v12, s13, v250
	v_pk_mul_f32 v[10:11], v[18:19], v[10:11]
	v_exp_f32_e64 v18, -v158
	v_exp_f32_e64 v19, -v159
	v_med3_f32 v12, v13, s13, v250
	v_med3_f32 v13, v10, s13, v250
	v_mov_b32_e32 v10, v35
	v_pk_add_f32 v[18:19], v[18:19], 1.0 op_sel_hi:[1,0]
	v_cvt_pk_fp8_f32 v10, v7, v12
	v_rcp_f32_e32 v18, v18
	v_rcp_f32_e32 v19, v19
	v_med3_f32 v11, v11, s13, v250
	v_cvt_pk_fp8_f32 v10, v13, v11 op_sel:[0,0,1]
	v_med3_f32 v7, v16, s13, v250
	v_pk_mul_f32 v[14:15], v[18:19], v[14:15]
	v_exp_f32_e64 v18, -v148
	v_exp_f32_e64 v19, -v149
	v_med3_f32 v12, v17, s13, v250
	v_mov_b32_e32 v11, v35
	v_pk_mul_f32 v[16:17], v[148:149], v[116:117]
	v_pk_add_f32 v[18:19], v[18:19], 1.0 op_sel_hi:[1,0]
	v_cvt_pk_fp8_f32 v11, v7, v12
	v_rcp_f32_e32 v18, v18
	v_rcp_f32_e32 v19, v19
	v_mov_b32_e32 v2, v165
	s_lshl_b32 s14, s49, 8
	s_lshl_b32 s30, s48, 7
	v_pk_mul_f32 v[16:17], v[18:19], v[16:17]
	v_exp_f32_e64 v18, -v154
	v_exp_f32_e64 v19, -v155
	v_readlane_b32 s26, v253, 26
	v_med3_f32 v13, v14, s13, v250
	v_med3_f32 v14, v15, s13, v250
	s_or_b32 s30, s30, s74
	s_add_i32 s14, s14, s73
	v_readlane_b32 s27, v253, 27
	v_cvt_pk_fp8_f32 v11, v13, v14 op_sel:[0,0,1]
	v_pk_add_f32 v[18:19], v[18:19], 1.0 op_sel_hi:[1,0]
	v_lshl_add_u32 v2, v2, 3, s30
	v_add_u32_e32 v6, s14, v3
	v_mov_b64_e32 v[4:5], s[26:27]
	s_movk_i32 s14, 0xe00
	v_rcp_f32_e32 v18, v18
	v_rcp_f32_e32 v19, v19
	v_ashrrev_i32_e32 v3, 31, v2
	v_mad_i64_i32 v[8:9], s[30:31], v6, s14, v[4:5]
	v_lshl_add_u64 v[8:9], v[8:9], 0, v[2:3]
	global_store_dwordx2 v[8:9], v[10:11], off
	v_pk_mul_f32 v[10:11], v[154:155], v[122:123]
	v_exp_f32_e64 v14, -v152
	v_exp_f32_e64 v15, -v153
	v_pk_mul_f32 v[10:11], v[18:19], v[10:11]
	v_exp_f32_e64 v18, -v150
	v_exp_f32_e64 v19, -v151
	v_pk_add_f32 v[14:15], v[14:15], 1.0 op_sel_hi:[1,0]
	v_pk_mul_f32 v[12:13], v[152:153], v[120:121]
	v_rcp_f32_e32 v14, v14
	v_rcp_f32_e32 v15, v15
	v_pk_add_f32 v[18:19], v[18:19], 1.0 op_sel_hi:[1,0]
	v_add_u32_e32 v7, 16, v6
	v_rcp_f32_e32 v18, v18
	v_rcp_f32_e32 v19, v19
	v_pk_mul_f32 v[12:13], v[14:15], v[12:13]
	v_pk_mul_f32 v[14:15], v[150:151], v[118:119]
	v_mad_i64_i32 v[8:9], s[30:31], v7, s14, v[4:5]
	v_pk_mul_f32 v[14:15], v[18:19], v[14:15]
	v_exp_f32_e64 v18, -v140
	v_exp_f32_e64 v19, -v141
	v_med3_f32 v7, v12, s13, v250
	v_med3_f32 v12, v13, s13, v250
	v_med3_f32 v13, v10, s13, v250
	v_mov_b32_e32 v10, v35
	v_cvt_pk_fp8_f32 v10, v7, v12
	v_pk_add_f32 v[18:19], v[18:19], 1.0 op_sel_hi:[1,0]
	v_med3_f32 v11, v11, s13, v250
	v_rcp_f32_e32 v18, v18
	v_rcp_f32_e32 v19, v19
	v_cvt_pk_fp8_f32 v10, v13, v11 op_sel:[0,0,1]
	v_med3_f32 v7, v16, s13, v250
	v_med3_f32 v12, v17, s13, v250
	v_mov_b32_e32 v11, v35
	v_pk_mul_f32 v[16:17], v[140:141], v[108:109]
	v_cvt_pk_fp8_f32 v11, v7, v12
	v_pk_mul_f32 v[16:17], v[18:19], v[16:17]
	v_exp_f32_e64 v18, -v146
	v_exp_f32_e64 v19, -v147
	v_med3_f32 v13, v14, s13, v250
	v_med3_f32 v14, v15, s13, v250
	v_cvt_pk_fp8_f32 v11, v13, v14 op_sel:[0,0,1]
	v_pk_add_f32 v[18:19], v[18:19], 1.0 op_sel_hi:[1,0]
	v_lshl_add_u64 v[8:9], v[8:9], 0, v[2:3]
	v_rcp_f32_e32 v18, v18
	v_rcp_f32_e32 v19, v19
	global_store_dwordx2 v[8:9], v[10:11], off
	s_and_b64 vcc, exec, s[16:17]
	s_cbranch_vccz .Lepi_nobar_0
	s_barrier
.Lepi_nobar_0:
	v_pk_mul_f32 v[10:11], v[146:147], v[114:115]
	v_exp_f32_e64 v14, -v144
	v_exp_f32_e64 v15, -v145
	v_pk_mul_f32 v[10:11], v[18:19], v[10:11]
	v_exp_f32_e64 v18, -v142
	v_exp_f32_e64 v19, -v143
	v_pk_add_f32 v[14:15], v[14:15], 1.0 op_sel_hi:[1,0]
	v_pk_mul_f32 v[12:13], v[144:145], v[112:113]
	v_rcp_f32_e32 v14, v14
	v_rcp_f32_e32 v15, v15
	v_pk_add_f32 v[18:19], v[18:19], 1.0 op_sel_hi:[1,0]
	v_add_u32_e32 v7, 32, v6
	v_rcp_f32_e32 v18, v18
	v_rcp_f32_e32 v19, v19
	v_pk_mul_f32 v[12:13], v[14:15], v[12:13]
	v_pk_mul_f32 v[14:15], v[142:143], v[110:111]
	v_mad_i64_i32 v[8:9], s[30:31], v7, s14, v[4:5]
	v_pk_mul_f32 v[14:15], v[18:19], v[14:15]
	v_exp_f32_e64 v18, -v132
	v_exp_f32_e64 v19, -v133
	v_med3_f32 v7, v12, s13, v250
	v_med3_f32 v12, v13, s13, v250
	v_med3_f32 v13, v10, s13, v250
	v_mov_b32_e32 v10, v35
	v_cvt_pk_fp8_f32 v10, v7, v12
	v_pk_add_f32 v[18:19], v[18:19], 1.0 op_sel_hi:[1,0]
	v_med3_f32 v11, v11, s13, v250
	v_rcp_f32_e32 v18, v18
	v_rcp_f32_e32 v19, v19
	v_cvt_pk_fp8_f32 v10, v13, v11 op_sel:[0,0,1]
	v_med3_f32 v7, v16, s13, v250
	v_med3_f32 v12, v17, s13, v250
	v_mov_b32_e32 v11, v35
	v_pk_mul_f32 v[16:17], v[132:133], v[100:101]
	v_cvt_pk_fp8_f32 v11, v7, v12
	v_pk_mul_f32 v[16:17], v[18:19], v[16:17]
	v_exp_f32_e64 v18, -v138
	v_exp_f32_e64 v19, -v139
	v_med3_f32 v13, v14, s13, v250
	v_med3_f32 v14, v15, s13, v250
	v_cvt_pk_fp8_f32 v11, v13, v14 op_sel:[0,0,1]
	v_pk_add_f32 v[18:19], v[18:19], 1.0 op_sel_hi:[1,0]
	v_lshl_add_u64 v[8:9], v[8:9], 0, v[2:3]
	v_rcp_f32_e32 v18, v18
	v_rcp_f32_e32 v19, v19
	global_store_dwordx2 v[8:9], v[10:11], off
	v_pk_mul_f32 v[10:11], v[138:139], v[106:107]
	v_exp_f32_e64 v14, -v136
	v_exp_f32_e64 v15, -v137
	v_pk_mul_f32 v[10:11], v[18:19], v[10:11]
	v_exp_f32_e64 v18, -v134
	v_exp_f32_e64 v19, -v135
	v_pk_add_f32 v[14:15], v[14:15], 1.0 op_sel_hi:[1,0]
	v_pk_mul_f32 v[12:13], v[136:137], v[104:105]
	v_rcp_f32_e32 v14, v14
	v_rcp_f32_e32 v15, v15
	v_pk_add_f32 v[18:19], v[18:19], 1.0 op_sel_hi:[1,0]
	v_add_u32_e32 v7, 48, v6
	v_rcp_f32_e32 v18, v18
	v_rcp_f32_e32 v19, v19
	v_pk_mul_f32 v[12:13], v[14:15], v[12:13]
	v_pk_mul_f32 v[14:15], v[134:135], v[102:103]
	v_mad_i64_i32 v[8:9], s[30:31], v7, s14, v[4:5]
	v_pk_mul_f32 v[14:15], v[18:19], v[14:15]
	v_exp_f32_e64 v18, -v92
	v_exp_f32_e64 v19, -v93
	v_med3_f32 v7, v12, s13, v250
	v_med3_f32 v12, v13, s13, v250
	v_med3_f32 v13, v10, s13, v250
	v_mov_b32_e32 v10, v35
	v_cvt_pk_fp8_f32 v10, v7, v12
	v_pk_add_f32 v[18:19], v[18:19], 1.0 op_sel_hi:[1,0]
	v_med3_f32 v11, v11, s13, v250
	v_rcp_f32_e32 v18, v18
	v_rcp_f32_e32 v19, v19
	v_cvt_pk_fp8_f32 v10, v13, v11 op_sel:[0,0,1]
	v_med3_f32 v7, v16, s13, v250
	v_med3_f32 v12, v17, s13, v250
	v_mov_b32_e32 v11, v35
	v_pk_mul_f32 v[16:17], v[92:93], v[60:61]
	v_cvt_pk_fp8_f32 v11, v7, v12
	v_pk_mul_f32 v[16:17], v[18:19], v[16:17]
	v_exp_f32_e64 v18, -v98
	v_exp_f32_e64 v19, -v99
	v_med3_f32 v13, v14, s13, v250
	v_med3_f32 v14, v15, s13, v250
	v_cvt_pk_fp8_f32 v11, v13, v14 op_sel:[0,0,1]
	v_pk_add_f32 v[18:19], v[18:19], 1.0 op_sel_hi:[1,0]
	v_lshl_add_u64 v[8:9], v[8:9], 0, v[2:3]
	v_rcp_f32_e32 v18, v18
	v_rcp_f32_e32 v19, v19
	global_store_dwordx2 v[8:9], v[10:11], off
	v_pk_mul_f32 v[10:11], v[98:99], v[66:67]
	v_exp_f32_e64 v14, -v96
	v_exp_f32_e64 v15, -v97
	v_pk_mul_f32 v[10:11], v[18:19], v[10:11]
	v_exp_f32_e64 v18, -v94
	v_exp_f32_e64 v19, -v95
	v_pk_add_f32 v[14:15], v[14:15], 1.0 op_sel_hi:[1,0]
	v_pk_mul_f32 v[12:13], v[96:97], v[64:65]
	v_rcp_f32_e32 v14, v14
	v_rcp_f32_e32 v15, v15
	v_pk_add_f32 v[18:19], v[18:19], 1.0 op_sel_hi:[1,0]
	v_add_u32_e32 v7, 0x80, v6
	v_rcp_f32_e32 v18, v18
	v_rcp_f32_e32 v19, v19
	v_pk_mul_f32 v[12:13], v[14:15], v[12:13]
	v_pk_mul_f32 v[14:15], v[94:95], v[62:63]
	v_mad_i64_i32 v[8:9], s[30:31], v7, s14, v[4:5]
	v_pk_mul_f32 v[14:15], v[18:19], v[14:15]
	v_exp_f32_e64 v18, -v84
	v_exp_f32_e64 v19, -v85
	v_med3_f32 v7, v12, s13, v250
	v_med3_f32 v12, v13, s13, v250
	v_med3_f32 v13, v10, s13, v250
	v_mov_b32_e32 v10, v35
	v_cvt_pk_fp8_f32 v10, v7, v12
	v_pk_add_f32 v[18:19], v[18:19], 1.0 op_sel_hi:[1,0]
	v_med3_f32 v11, v11, s13, v250
	v_rcp_f32_e32 v18, v18
	v_rcp_f32_e32 v19, v19
	v_cvt_pk_fp8_f32 v10, v13, v11 op_sel:[0,0,1]
	v_med3_f32 v7, v16, s13, v250
	v_med3_f32 v12, v17, s13, v250
	v_mov_b32_e32 v11, v35
	v_pk_mul_f32 v[16:17], v[84:85], v[52:53]
	v_cvt_pk_fp8_f32 v11, v7, v12
	v_pk_mul_f32 v[16:17], v[18:19], v[16:17]
	v_exp_f32_e64 v18, -v90
	v_exp_f32_e64 v19, -v91
	v_med3_f32 v13, v14, s13, v250
	v_med3_f32 v14, v15, s13, v250
	v_cvt_pk_fp8_f32 v11, v13, v14 op_sel:[0,0,1]
	v_pk_add_f32 v[18:19], v[18:19], 1.0 op_sel_hi:[1,0]
	v_lshl_add_u64 v[8:9], v[8:9], 0, v[2:3]
	v_rcp_f32_e32 v18, v18
	v_rcp_f32_e32 v19, v19
	v_exp_f32_e64 v14, -v88
	v_exp_f32_e64 v15, -v89
	global_store_dwordx2 v[8:9], v[10:11], off
	v_pk_mul_f32 v[10:11], v[90:91], v[58:59]
	v_pk_mul_f32 v[12:13], v[88:89], v[56:57]
	v_pk_mul_f32 v[10:11], v[18:19], v[10:11]
	v_exp_f32_e64 v18, -v86
	v_exp_f32_e64 v19, -v87
	v_pk_add_f32 v[14:15], v[14:15], 1.0 op_sel_hi:[1,0]
	v_add_u32_e32 v7, 0x90, v6
	v_rcp_f32_e32 v14, v14
	v_rcp_f32_e32 v15, v15
	v_pk_add_f32 v[18:19], v[18:19], 1.0 op_sel_hi:[1,0]
	v_mad_i64_i32 v[8:9], s[30:31], v7, s14, v[4:5]
	v_rcp_f32_e32 v18, v18
	v_rcp_f32_e32 v19, v19
	v_pk_mul_f32 v[12:13], v[14:15], v[12:13]
	v_pk_mul_f32 v[14:15], v[86:87], v[54:55]
	v_med3_f32 v7, v12, s13, v250
	v_med3_f32 v12, v13, s13, v250
	v_med3_f32 v13, v10, s13, v250
	v_mov_b32_e32 v10, v35
	v_pk_mul_f32 v[14:15], v[18:19], v[14:15]
	v_cvt_pk_fp8_f32 v10, v7, v12
	v_exp_f32_e64 v18, -v76
	v_exp_f32_e64 v19, -v77
	v_med3_f32 v11, v11, s13, v250
	v_cvt_pk_fp8_f32 v10, v13, v11 op_sel:[0,0,1]
	v_med3_f32 v7, v16, s13, v250
	v_med3_f32 v12, v17, s13, v250
	v_mov_b32_e32 v11, v35
	v_pk_add_f32 v[18:19], v[18:19], 1.0 op_sel_hi:[1,0]
	v_cvt_pk_fp8_f32 v11, v7, v12
	v_rcp_f32_e32 v18, v18
	v_rcp_f32_e32 v19, v19
	v_med3_f32 v13, v14, s13, v250
	v_med3_f32 v14, v15, s13, v250
	v_pk_mul_f32 v[16:17], v[76:77], v[44:45]
	v_cvt_pk_fp8_f32 v11, v13, v14 op_sel:[0,0,1]
	v_exp_f32_e64 v14, -v80
	v_exp_f32_e64 v15, -v81
	v_pk_mul_f32 v[16:17], v[18:19], v[16:17]
	v_exp_f32_e64 v18, -v82
	v_exp_f32_e64 v19, -v83
	v_pk_add_f32 v[14:15], v[14:15], 1.0 op_sel_hi:[1,0]
	v_lshl_add_u64 v[8:9], v[8:9], 0, v[2:3]
	v_rcp_f32_e32 v14, v14
	v_pk_add_f32 v[18:19], v[18:19], 1.0 op_sel_hi:[1,0]
	v_rcp_f32_e32 v15, v15
	v_rcp_f32_e32 v18, v18
	v_rcp_f32_e32 v19, v19
	global_store_dwordx2 v[8:9], v[10:11], off
	v_pk_mul_f32 v[10:11], v[82:83], v[50:51]
	v_pk_mul_f32 v[12:13], v[80:81], v[48:49]
	v_add_u32_e32 v7, 0xa0, v6
	v_pk_mul_f32 v[12:13], v[14:15], v[12:13]
	v_pk_mul_f32 v[10:11], v[18:19], v[10:11]
	v_exp_f32_e64 v18, -v78
	v_exp_f32_e64 v19, -v79
	v_mad_i64_i32 v[8:9], s[30:31], v7, s14, v[4:5]
	v_med3_f32 v7, v12, s13, v250
	v_med3_f32 v12, v13, s13, v250
	v_med3_f32 v13, v10, s13, v250
	v_mov_b32_e32 v10, v35
	v_cvt_pk_fp8_f32 v10, v7, v12
	v_pk_add_f32 v[18:19], v[18:19], 1.0 op_sel_hi:[1,0]
	v_med3_f32 v11, v11, s13, v250
	v_rcp_f32_e32 v18, v18
	v_rcp_f32_e32 v19, v19
	v_cvt_pk_fp8_f32 v10, v13, v11 op_sel:[0,0,1]
	v_med3_f32 v7, v16, s13, v250
	v_med3_f32 v12, v17, s13, v250
	v_mov_b32_e32 v11, v35
	v_cvt_pk_fp8_f32 v11, v7, v12
	v_pk_mul_f32 v[14:15], v[78:79], v[46:47]
	v_lshl_add_u64 v[8:9], v[8:9], 0, v[2:3]
	v_pk_mul_f32 v[14:15], v[18:19], v[14:15]
	v_add_u32_e32 v6, 0xb0, v6
	v_med3_f32 v13, v14, s13, v250
	v_med3_f32 v14, v15, s13, v250
	v_cvt_pk_fp8_f32 v11, v13, v14 op_sel:[0,0,1]
	v_exp_f32_e64 v14, -v68
	v_exp_f32_e64 v15, -v69
	v_pk_mul_f32 v[12:13], v[68:69], v[36:37]
	global_store_dwordx2 v[8:9], v[10:11], off
	v_exp_f32_e64 v10, -v72
	v_pk_add_f32 v[14:15], v[14:15], 1.0 op_sel_hi:[1,0]
	v_exp_f32_e64 v11, -v73
	v_rcp_f32_e32 v14, v14
	v_rcp_f32_e32 v15, v15
	v_mad_i64_i32 v[4:5], s[30:31], v6, s14, v[4:5]
	v_pk_add_f32 v[10:11], v[10:11], 1.0 op_sel_hi:[1,0]
	v_pk_mul_f32 v[12:13], v[14:15], v[12:13]
	v_exp_f32_e64 v14, -v74
	v_exp_f32_e64 v15, -v75
	v_rcp_f32_e32 v10, v10
	v_rcp_f32_e32 v11, v11
	v_pk_mul_f32 v[6:7], v[74:75], v[42:43]
	v_pk_add_f32 v[14:15], v[14:15], 1.0 op_sel_hi:[1,0]
	v_pk_mul_f32 v[8:9], v[72:73], v[40:41]
	v_rcp_f32_e32 v14, v14
	v_rcp_f32_e32 v15, v15
	v_pk_mul_f32 v[8:9], v[10:11], v[8:9]
	v_lshl_add_u64 v[2:3], v[4:5], 0, v[2:3]
	v_med3_f32 v5, v8, s13, v250
	v_pk_mul_f32 v[6:7], v[14:15], v[6:7]
	v_exp_f32_e64 v14, -v70
	v_exp_f32_e64 v15, -v71
	v_med3_f32 v8, v9, s13, v250
	v_mov_b32_e32 v4, v35
	v_cvt_pk_fp8_f32 v4, v5, v8
	v_pk_add_f32 v[14:15], v[14:15], 1.0 op_sel_hi:[1,0]
	v_med3_f32 v6, v6, s13, v250
	v_rcp_f32_e32 v14, v14
	v_rcp_f32_e32 v15, v15
	v_med3_f32 v7, v7, s13, v250
	v_cvt_pk_fp8_f32 v4, v6, v7 op_sel:[0,0,1]
	v_med3_f32 v6, v12, s13, v250
	v_med3_f32 v7, v13, s13, v250
	v_mov_b32_e32 v5, v35
	v_cvt_pk_fp8_f32 v5, v6, v7
	v_pk_mul_f32 v[10:11], v[70:71], v[38:39]
	s_and_b64 vcc, exec, s[6:7]
	v_pk_mul_f32 v[10:11], v[14:15], v[10:11]
	s_mov_b64 s[84:85], s[24:25]
	v_med3_f32 v8, v10, s13, v250
	v_med3_f32 v9, v11, s13, v250
	v_cvt_pk_fp8_f32 v5, v8, v9 op_sel:[0,0,1]
	global_store_dwordx2 v[2:3], v[4:5], off
	s_cbranch_vccnz .LBB0_828
	s_andn2_b64 vcc, exec, s[10:11]
	s_cbranch_vccnz .LBB0_810
	s_barrier
	s_branch .LBB0_810

.LBB0_957:
.LBB0_959:
	v_exp_f32_e64 v18, -v156
	v_exp_f32_e64 v19, -v157
	v_pk_mul_f32 v[16:17], v[156:157], v[124:125]
	v_pk_mul_f32 v[10:11], v[162:163], v[130:131]
	v_exp_f32_e64 v14, -v160
	v_pk_add_f32 v[18:19], v[18:19], 1.0 op_sel_hi:[1,0]
	v_exp_f32_e64 v15, -v161
	v_rcp_f32_e32 v18, v18
	v_rcp_f32_e32 v19, v19
	v_pk_mul_f32 v[12:13], v[160:161], v[128:129]
	v_pk_add_f32 v[14:15], v[14:15], 1.0 op_sel_hi:[1,0]
	s_add_u32 s30, s95, 0xfffffe00
	v_pk_mul_f32 v[16:17], v[18:19], v[16:17]
	v_exp_f32_e64 v18, -v162
	v_exp_f32_e64 v19, -v163
	v_rcp_f32_e32 v14, v14
	v_rcp_f32_e32 v15, v15
	s_addc_u32 s31, s96, -1
	v_pk_add_f32 v[18:19], v[18:19], 1.0 op_sel_hi:[1,0]
	v_mov_b32_e32 v3, v1
	v_rcp_f32_e32 v18, v18
	v_rcp_f32_e32 v19, v19
	v_pk_mul_f32 v[12:13], v[14:15], v[12:13]
	v_pk_mul_f32 v[14:15], v[158:159], v[126:127]
	v_med3_f32 v7, v12, s13, v250
	v_pk_mul_f32 v[10:11], v[18:19], v[10:11]
	v_exp_f32_e64 v18, -v158
	v_exp_f32_e64 v19, -v159
	v_med3_f32 v12, v13, s13, v250
	v_med3_f32 v13, v10, s13, v250
	v_mov_b32_e32 v10, v35
	v_pk_add_f32 v[18:19], v[18:19], 1.0 op_sel_hi:[1,0]
	v_cvt_pk_fp8_f32 v10, v7, v12
	v_rcp_f32_e32 v18, v18
	v_rcp_f32_e32 v19, v19
	v_med3_f32 v11, v11, s13, v250
	v_cvt_pk_fp8_f32 v10, v13, v11 op_sel:[0,0,1]
	v_med3_f32 v7, v16, s13, v250
	v_pk_mul_f32 v[14:15], v[18:19], v[14:15]
	v_exp_f32_e64 v18, -v148
	v_exp_f32_e64 v19, -v149
	v_med3_f32 v12, v17, s13, v250
	v_mov_b32_e32 v11, v35
	v_pk_mul_f32 v[16:17], v[148:149], v[116:117]
	v_pk_add_f32 v[18:19], v[18:19], 1.0 op_sel_hi:[1,0]
	v_cvt_pk_fp8_f32 v11, v7, v12
	v_rcp_f32_e32 v18, v18
	v_rcp_f32_e32 v19, v19
	v_mov_b32_e32 v2, v165
	s_lshl_b32 s14, s77, 8
	s_lshl_b32 s46, s76, 7
	v_pk_mul_f32 v[16:17], v[18:19], v[16:17]
	v_exp_f32_e64 v18, -v154
	v_exp_f32_e64 v19, -v155
	v_med3_f32 v13, v14, s13, v250
	v_med3_f32 v14, v15, s13, v250
	s_or_b32 s46, s46, s89
	s_add_i32 s14, s14, s87
	v_cvt_pk_fp8_f32 v11, v13, v14 op_sel:[0,0,1]
	v_pk_add_f32 v[18:19], v[18:19], 1.0 op_sel_hi:[1,0]
	v_lshl_add_u32 v2, v2, 3, s46
	v_add_u32_e32 v6, s14, v3
	v_mov_b64_e32 v[4:5], s[22:23]
	s_movk_i32 s14, 0xe00
	v_rcp_f32_e32 v18, v18
	v_rcp_f32_e32 v19, v19
	v_ashrrev_i32_e32 v3, 31, v2
	v_mad_i64_i32 v[8:9], s[46:47], v6, s14, v[4:5]
	v_lshl_add_u64 v[8:9], v[8:9], 0, v[2:3]
	global_store_dwordx2 v[8:9], v[10:11], off
	v_pk_mul_f32 v[10:11], v[154:155], v[122:123]
	v_exp_f32_e64 v14, -v152
	v_exp_f32_e64 v15, -v153
	v_pk_mul_f32 v[10:11], v[18:19], v[10:11]
	v_exp_f32_e64 v18, -v150
	v_exp_f32_e64 v19, -v151
	v_pk_add_f32 v[14:15], v[14:15], 1.0 op_sel_hi:[1,0]
	v_pk_mul_f32 v[12:13], v[152:153], v[120:121]
	v_rcp_f32_e32 v14, v14
	v_rcp_f32_e32 v15, v15
	v_pk_add_f32 v[18:19], v[18:19], 1.0 op_sel_hi:[1,0]
	v_add_u32_e32 v7, 16, v6
	v_rcp_f32_e32 v18, v18
	v_rcp_f32_e32 v19, v19
	v_pk_mul_f32 v[12:13], v[14:15], v[12:13]
	v_pk_mul_f32 v[14:15], v[150:151], v[118:119]
	v_mad_i64_i32 v[8:9], s[46:47], v7, s14, v[4:5]
	v_pk_mul_f32 v[14:15], v[18:19], v[14:15]
	v_exp_f32_e64 v18, -v140
	v_exp_f32_e64 v19, -v141
	v_med3_f32 v7, v12, s13, v250
	v_med3_f32 v12, v13, s13, v250
	v_med3_f32 v13, v10, s13, v250
	v_mov_b32_e32 v10, v35
	v_cvt_pk_fp8_f32 v10, v7, v12
	v_pk_add_f32 v[18:19], v[18:19], 1.0 op_sel_hi:[1,0]
	v_med3_f32 v11, v11, s13, v250
	v_rcp_f32_e32 v18, v18
	v_rcp_f32_e32 v19, v19
	v_cvt_pk_fp8_f32 v10, v13, v11 op_sel:[0,0,1]
	v_med3_f32 v7, v16, s13, v250
	v_med3_f32 v12, v17, s13, v250
	v_mov_b32_e32 v11, v35
	v_pk_mul_f32 v[16:17], v[140:141], v[108:109]
	v_cvt_pk_fp8_f32 v11, v7, v12
	v_pk_mul_f32 v[16:17], v[18:19], v[16:17]
	v_exp_f32_e64 v18, -v146
	v_exp_f32_e64 v19, -v147
	v_med3_f32 v13, v14, s13, v250
	v_med3_f32 v14, v15, s13, v250
	v_cvt_pk_fp8_f32 v11, v13, v14 op_sel:[0,0,1]
	v_pk_add_f32 v[18:19], v[18:19], 1.0 op_sel_hi:[1,0]
	v_lshl_add_u64 v[8:9], v[8:9], 0, v[2:3]
	v_rcp_f32_e32 v18, v18
	v_rcp_f32_e32 v19, v19
	global_store_dwordx2 v[8:9], v[10:11], off
	s_and_b64 vcc, exec, s[36:37]
	s_cbranch_vccz .Lepi_nobar_1
	s_barrier
.Lepi_nobar_1:
	v_pk_mul_f32 v[10:11], v[146:147], v[114:115]
	v_exp_f32_e64 v14, -v144
	v_exp_f32_e64 v15, -v145
	v_pk_mul_f32 v[10:11], v[18:19], v[10:11]
	v_exp_f32_e64 v18, -v142
	v_exp_f32_e64 v19, -v143
	v_pk_add_f32 v[14:15], v[14:15], 1.0 op_sel_hi:[1,0]
	v_pk_mul_f32 v[12:13], v[144:145], v[112:113]
	v_rcp_f32_e32 v14, v14
	v_rcp_f32_e32 v15, v15
	v_pk_add_f32 v[18:19], v[18:19], 1.0 op_sel_hi:[1,0]
	v_add_u32_e32 v7, 32, v6
	v_rcp_f32_e32 v18, v18
	v_rcp_f32_e32 v19, v19
	v_pk_mul_f32 v[12:13], v[14:15], v[12:13]
	v_pk_mul_f32 v[14:15], v[142:143], v[110:111]
	v_mad_i64_i32 v[8:9], s[46:47], v7, s14, v[4:5]
	v_pk_mul_f32 v[14:15], v[18:19], v[14:15]
	v_exp_f32_e64 v18, -v132
	v_exp_f32_e64 v19, -v133
	v_med3_f32 v7, v12, s13, v250
	v_med3_f32 v12, v13, s13, v250
	v_med3_f32 v13, v10, s13, v250
	v_mov_b32_e32 v10, v35
	v_cvt_pk_fp8_f32 v10, v7, v12
	v_pk_add_f32 v[18:19], v[18:19], 1.0 op_sel_hi:[1,0]
	v_med3_f32 v11, v11, s13, v250
	v_rcp_f32_e32 v18, v18
	v_rcp_f32_e32 v19, v19
	v_cvt_pk_fp8_f32 v10, v13, v11 op_sel:[0,0,1]
	v_med3_f32 v7, v16, s13, v250
	v_med3_f32 v12, v17, s13, v250
	v_mov_b32_e32 v11, v35
	v_pk_mul_f32 v[16:17], v[132:133], v[100:101]
	v_cvt_pk_fp8_f32 v11, v7, v12
	v_pk_mul_f32 v[16:17], v[18:19], v[16:17]
	v_exp_f32_e64 v18, -v138
	v_exp_f32_e64 v19, -v139
	v_med3_f32 v13, v14, s13, v250
	v_med3_f32 v14, v15, s13, v250
	v_cvt_pk_fp8_f32 v11, v13, v14 op_sel:[0,0,1]
	v_pk_add_f32 v[18:19], v[18:19], 1.0 op_sel_hi:[1,0]
	v_lshl_add_u64 v[8:9], v[8:9], 0, v[2:3]
	v_rcp_f32_e32 v18, v18
	v_rcp_f32_e32 v19, v19
	global_store_dwordx2 v[8:9], v[10:11], off
	v_pk_mul_f32 v[10:11], v[138:139], v[106:107]
	v_exp_f32_e64 v14, -v136
	v_exp_f32_e64 v15, -v137
	v_pk_mul_f32 v[10:11], v[18:19], v[10:11]
	v_exp_f32_e64 v18, -v134
	v_exp_f32_e64 v19, -v135
	v_pk_add_f32 v[14:15], v[14:15], 1.0 op_sel_hi:[1,0]
	v_pk_mul_f32 v[12:13], v[136:137], v[104:105]
	v_rcp_f32_e32 v14, v14
	v_rcp_f32_e32 v15, v15
	v_pk_add_f32 v[18:19], v[18:19], 1.0 op_sel_hi:[1,0]
	v_add_u32_e32 v7, 48, v6
	v_rcp_f32_e32 v18, v18
	v_rcp_f32_e32 v19, v19
	v_pk_mul_f32 v[12:13], v[14:15], v[12:13]
	v_pk_mul_f32 v[14:15], v[134:135], v[102:103]
	v_mad_i64_i32 v[8:9], s[46:47], v7, s14, v[4:5]
	v_pk_mul_f32 v[14:15], v[18:19], v[14:15]
	v_exp_f32_e64 v18, -v92
	v_exp_f32_e64 v19, -v93
	v_med3_f32 v7, v12, s13, v250
	v_med3_f32 v12, v13, s13, v250
	v_med3_f32 v13, v10, s13, v250
	v_mov_b32_e32 v10, v35
	v_cvt_pk_fp8_f32 v10, v7, v12
	v_pk_add_f32 v[18:19], v[18:19], 1.0 op_sel_hi:[1,0]
	v_med3_f32 v11, v11, s13, v250
	v_rcp_f32_e32 v18, v18
	v_rcp_f32_e32 v19, v19
	v_cvt_pk_fp8_f32 v10, v13, v11 op_sel:[0,0,1]
	v_med3_f32 v7, v16, s13, v250
	v_med3_f32 v12, v17, s13, v250
	v_mov_b32_e32 v11, v35
	v_pk_mul_f32 v[16:17], v[92:93], v[60:61]
	v_cvt_pk_fp8_f32 v11, v7, v12
	v_pk_mul_f32 v[16:17], v[18:19], v[16:17]
	v_exp_f32_e64 v18, -v98
	v_exp_f32_e64 v19, -v99
	v_med3_f32 v13, v14, s13, v250
	v_med3_f32 v14, v15, s13, v250
	v_cvt_pk_fp8_f32 v11, v13, v14 op_sel:[0,0,1]
	v_pk_add_f32 v[18:19], v[18:19], 1.0 op_sel_hi:[1,0]
	v_lshl_add_u64 v[8:9], v[8:9], 0, v[2:3]
	v_rcp_f32_e32 v18, v18
	v_rcp_f32_e32 v19, v19
	global_store_dwordx2 v[8:9], v[10:11], off
	v_pk_mul_f32 v[10:11], v[98:99], v[66:67]
	v_exp_f32_e64 v14, -v96
	v_exp_f32_e64 v15, -v97
	v_pk_mul_f32 v[10:11], v[18:19], v[10:11]
	v_exp_f32_e64 v18, -v94
	v_exp_f32_e64 v19, -v95
	v_pk_add_f32 v[14:15], v[14:15], 1.0 op_sel_hi:[1,0]
	v_pk_mul_f32 v[12:13], v[96:97], v[64:65]
	v_rcp_f32_e32 v14, v14
	v_rcp_f32_e32 v15, v15
	v_pk_add_f32 v[18:19], v[18:19], 1.0 op_sel_hi:[1,0]
	v_add_u32_e32 v7, 0x80, v6
	v_rcp_f32_e32 v18, v18
	v_rcp_f32_e32 v19, v19
	v_pk_mul_f32 v[12:13], v[14:15], v[12:13]
	v_pk_mul_f32 v[14:15], v[94:95], v[62:63]
	v_mad_i64_i32 v[8:9], s[46:47], v7, s14, v[4:5]
	v_pk_mul_f32 v[14:15], v[18:19], v[14:15]
	v_exp_f32_e64 v18, -v84
	v_exp_f32_e64 v19, -v85
	v_med3_f32 v7, v12, s13, v250
	v_med3_f32 v12, v13, s13, v250
	v_med3_f32 v13, v10, s13, v250
	v_mov_b32_e32 v10, v35
	v_cvt_pk_fp8_f32 v10, v7, v12
	v_pk_add_f32 v[18:19], v[18:19], 1.0 op_sel_hi:[1,0]
	v_med3_f32 v11, v11, s13, v250
	v_rcp_f32_e32 v18, v18
	v_rcp_f32_e32 v19, v19
	v_cvt_pk_fp8_f32 v10, v13, v11 op_sel:[0,0,1]
	v_med3_f32 v7, v16, s13, v250
	v_med3_f32 v12, v17, s13, v250
	v_mov_b32_e32 v11, v35
	v_pk_mul_f32 v[16:17], v[84:85], v[52:53]
	v_cvt_pk_fp8_f32 v11, v7, v12
	v_pk_mul_f32 v[16:17], v[18:19], v[16:17]
	v_exp_f32_e64 v18, -v90
	v_exp_f32_e64 v19, -v91
	v_med3_f32 v13, v14, s13, v250
	v_med3_f32 v14, v15, s13, v250
	v_cvt_pk_fp8_f32 v11, v13, v14 op_sel:[0,0,1]
	v_pk_add_f32 v[18:19], v[18:19], 1.0 op_sel_hi:[1,0]
	v_lshl_add_u64 v[8:9], v[8:9], 0, v[2:3]
	v_rcp_f32_e32 v18, v18
	v_rcp_f32_e32 v19, v19
	v_exp_f32_e64 v14, -v88
	v_exp_f32_e64 v15, -v89
	global_store_dwordx2 v[8:9], v[10:11], off
	v_pk_mul_f32 v[10:11], v[90:91], v[58:59]
	v_pk_mul_f32 v[12:13], v[88:89], v[56:57]
	v_pk_mul_f32 v[10:11], v[18:19], v[10:11]
	v_exp_f32_e64 v18, -v86
	v_exp_f32_e64 v19, -v87
	v_pk_add_f32 v[14:15], v[14:15], 1.0 op_sel_hi:[1,0]
	v_add_u32_e32 v7, 0x90, v6
	v_rcp_f32_e32 v14, v14
	v_rcp_f32_e32 v15, v15
	v_pk_add_f32 v[18:19], v[18:19], 1.0 op_sel_hi:[1,0]
	v_mad_i64_i32 v[8:9], s[46:47], v7, s14, v[4:5]
	v_rcp_f32_e32 v18, v18
	v_rcp_f32_e32 v19, v19
	v_pk_mul_f32 v[12:13], v[14:15], v[12:13]
	v_pk_mul_f32 v[14:15], v[86:87], v[54:55]
	v_med3_f32 v7, v12, s13, v250
	v_med3_f32 v12, v13, s13, v250
	v_med3_f32 v13, v10, s13, v250
	v_mov_b32_e32 v10, v35
	v_pk_mul_f32 v[14:15], v[18:19], v[14:15]
	v_cvt_pk_fp8_f32 v10, v7, v12
	v_exp_f32_e64 v18, -v76
	v_exp_f32_e64 v19, -v77
	v_med3_f32 v11, v11, s13, v250
	v_cvt_pk_fp8_f32 v10, v13, v11 op_sel:[0,0,1]
	v_med3_f32 v7, v16, s13, v250
	v_med3_f32 v12, v17, s13, v250
	v_mov_b32_e32 v11, v35
	v_pk_add_f32 v[18:19], v[18:19], 1.0 op_sel_hi:[1,0]
	v_cvt_pk_fp8_f32 v11, v7, v12
	v_rcp_f32_e32 v18, v18
	v_rcp_f32_e32 v19, v19
	v_med3_f32 v13, v14, s13, v250
	v_med3_f32 v14, v15, s13, v250
	v_pk_mul_f32 v[16:17], v[76:77], v[44:45]
	v_cvt_pk_fp8_f32 v11, v13, v14 op_sel:[0,0,1]
	v_exp_f32_e64 v14, -v80
	v_exp_f32_e64 v15, -v81
	v_pk_mul_f32 v[16:17], v[18:19], v[16:17]
	v_exp_f32_e64 v18, -v82
	v_exp_f32_e64 v19, -v83
	v_pk_add_f32 v[14:15], v[14:15], 1.0 op_sel_hi:[1,0]
	v_lshl_add_u64 v[8:9], v[8:9], 0, v[2:3]
	v_rcp_f32_e32 v14, v14
	v_pk_add_f32 v[18:19], v[18:19], 1.0 op_sel_hi:[1,0]
	v_rcp_f32_e32 v15, v15
	v_rcp_f32_e32 v18, v18
	v_rcp_f32_e32 v19, v19
	global_store_dwordx2 v[8:9], v[10:11], off
	v_pk_mul_f32 v[10:11], v[82:83], v[50:51]
	v_pk_mul_f32 v[12:13], v[80:81], v[48:49]
	v_add_u32_e32 v7, 0xa0, v6
	v_pk_mul_f32 v[12:13], v[14:15], v[12:13]
	v_pk_mul_f32 v[10:11], v[18:19], v[10:11]
	v_exp_f32_e64 v18, -v78
	v_exp_f32_e64 v19, -v79
	v_mad_i64_i32 v[8:9], s[46:47], v7, s14, v[4:5]
	v_med3_f32 v7, v12, s13, v250
	v_med3_f32 v12, v13, s13, v250
	v_med3_f32 v13, v10, s13, v250
	v_mov_b32_e32 v10, v35
	v_cvt_pk_fp8_f32 v10, v7, v12
	v_pk_add_f32 v[18:19], v[18:19], 1.0 op_sel_hi:[1,0]
	v_med3_f32 v11, v11, s13, v250
	v_rcp_f32_e32 v18, v18
	v_rcp_f32_e32 v19, v19
	v_cvt_pk_fp8_f32 v10, v13, v11 op_sel:[0,0,1]
	v_med3_f32 v7, v16, s13, v250
	v_med3_f32 v12, v17, s13, v250
	v_mov_b32_e32 v11, v35
	v_cvt_pk_fp8_f32 v11, v7, v12
	v_pk_mul_f32 v[14:15], v[78:79], v[46:47]
	v_lshl_add_u64 v[8:9], v[8:9], 0, v[2:3]
	v_pk_mul_f32 v[14:15], v[18:19], v[14:15]
	v_add_u32_e32 v6, 0xb0, v6
	v_med3_f32 v13, v14, s13, v250
	v_med3_f32 v14, v15, s13, v250
	v_cvt_pk_fp8_f32 v11, v13, v14 op_sel:[0,0,1]
	v_exp_f32_e64 v14, -v68
	v_exp_f32_e64 v15, -v69
	v_pk_mul_f32 v[12:13], v[68:69], v[36:37]
	global_store_dwordx2 v[8:9], v[10:11], off
	v_exp_f32_e64 v10, -v72
	v_pk_add_f32 v[14:15], v[14:15], 1.0 op_sel_hi:[1,0]
	v_exp_f32_e64 v11, -v73
	v_rcp_f32_e32 v14, v14
	v_rcp_f32_e32 v15, v15
	v_mad_i64_i32 v[4:5], s[46:47], v6, s14, v[4:5]
	v_pk_add_f32 v[10:11], v[10:11], 1.0 op_sel_hi:[1,0]
	v_pk_mul_f32 v[12:13], v[14:15], v[12:13]
	v_exp_f32_e64 v14, -v74
	v_exp_f32_e64 v15, -v75
	v_rcp_f32_e32 v10, v10
	v_rcp_f32_e32 v11, v11
	v_pk_mul_f32 v[6:7], v[74:75], v[42:43]
	v_pk_add_f32 v[14:15], v[14:15], 1.0 op_sel_hi:[1,0]
	v_pk_mul_f32 v[8:9], v[72:73], v[40:41]
	v_rcp_f32_e32 v14, v14
	v_rcp_f32_e32 v15, v15
	v_pk_mul_f32 v[8:9], v[10:11], v[8:9]
	v_lshl_add_u64 v[2:3], v[4:5], 0, v[2:3]
	v_med3_f32 v5, v8, s13, v250
	v_pk_mul_f32 v[6:7], v[14:15], v[6:7]
	v_exp_f32_e64 v14, -v70
	v_exp_f32_e64 v15, -v71
	v_med3_f32 v8, v9, s13, v250
	v_mov_b32_e32 v4, v35
	v_cvt_pk_fp8_f32 v4, v5, v8
	v_pk_add_f32 v[14:15], v[14:15], 1.0 op_sel_hi:[1,0]
	v_med3_f32 v6, v6, s13, v250
	v_rcp_f32_e32 v14, v14
	v_rcp_f32_e32 v15, v15
	v_med3_f32 v7, v7, s13, v250
	v_cvt_pk_fp8_f32 v4, v6, v7 op_sel:[0,0,1]
	v_med3_f32 v6, v12, s13, v250
	v_med3_f32 v7, v13, s13, v250
	v_mov_b32_e32 v5, v35
	v_cvt_pk_fp8_f32 v5, v6, v7
	v_pk_mul_f32 v[10:11], v[70:71], v[38:39]
	s_andn2_b64 vcc, exec, s[44:45]
	v_pk_mul_f32 v[10:11], v[14:15], v[10:11]
	s_nop 0
	v_med3_f32 v8, v10, s13, v250
	v_med3_f32 v9, v11, s13, v250
	v_cvt_pk_fp8_f32 v5, v8, v9 op_sel:[0,0,1]
	global_store_dwordx2 v[2:3], v[4:5], off
	s_cbranch_vccnz .LBB0_962
	v_readlane_b32 s96, v254, 55
	s_andn2_b64 vcc, exec, s[6:7]
	v_readlane_b32 s95, v254, 48
	v_readlane_b32 s97, v254, 56
	s_cbranch_vccnz .LBB0_935
	s_barrier
	s_branch .LBB0_935

.LBB0_982:
	v_readlane_b32 s6, v252, 62
	v_readlane_b32 s7, v252, 63
	v_cvt_f32_u32_e32 v1, v3
	v_sub_u32_e32 v5, 0, v3
	v_rcp_iflag_f32_e32 v1, v1
	s_nop 1
	global_atomic_add v4, v35, v246, s[6:7] sc0
	v_mul_f32_e32 v1, 0x4f7ffffe, v1
	v_cvt_u32_f32_e32 v1, v1
	v_mul_lo_u32 v5, v5, v1
	v_mul_hi_u32 v5, v1, v5
	v_add_u32_e32 v1, v1, v5
	s_waitcnt vmcnt(0)
	v_mul_hi_u32 v1, v4, v1
	v_mul_lo_u32 v5, v1, v3
	v_sub_u32_e32 v5, v4, v5
	v_add_u32_e32 v6, 1, v1
	v_cmp_ge_u32_e32 vcc, v5, v3
	v_add_u32_e32 v4, 1, v4
	s_nop 0
	v_cndmask_b32_e32 v1, v1, v6, vcc
	v_sub_u32_e32 v6, v5, v3
	v_cndmask_b32_e32 v5, v5, v6, vcc
	v_add_u32_e32 v6, 1, v1
	v_cmp_ge_u32_e32 vcc, v5, v3
	s_nop 1
	v_cndmask_b32_e32 v1, v1, v6, vcc
	v_mul_lo_u32 v5, v3, v1
	v_add_u32_e32 v3, v5, v3
	v_cmp_ne_u32_e32 vcc, v4, v3
	s_and_saveexec_b64 s[6:7], vcc
	s_xor_b64 s[6:7], exec, s[6:7]
	s_cbranch_execz .LBB0_996
	s_waitcnt lgkmcnt(0)
	v_readlane_b32 s98, v254, 57
	v_readlane_b32 s99, v254, 58
	s_nop 0
	s_add_u32 s98, s98, 0x3300
	s_addc_u32 s99, s99, 0
	s_nop 1
	global_load_dword v2, v35, s[98:99] sc1
	s_waitcnt vmcnt(0)
	v_cmp_eq_u32_e32 vcc, v2, v1
	s_and_saveexec_b64 s[10:11], vcc
	s_cbranch_execz .LBB0_995
	s_mov_b32 s15, 1
	s_mov_b64 s[16:17], 0
	s_branch .LBB0_986

.LBB0_988:
	global_load_dword v2, v35, s[98:99] sc1
	s_add_i32 s15, s15, 1
	s_mov_b64 s[36:37], -1
	s_waitcnt vmcnt(0)
	v_cmp_ne_u32_e32 vcc, v2, v1
	s_orn2_b64 s[30:31], vcc, exec
	s_branch .LBB0_985

.LBB0_1090:
	v_exp_f32_e64 v18, -v156
	v_exp_f32_e64 v19, -v157
	v_pk_mul_f32 v[16:17], v[156:157], v[124:125]
	v_pk_mul_f32 v[10:11], v[162:163], v[130:131]
	v_exp_f32_e64 v14, -v160
	v_pk_add_f32 v[18:19], v[18:19], 1.0 op_sel_hi:[1,0]
	v_exp_f32_e64 v15, -v161
	v_rcp_f32_e32 v18, v18
	v_rcp_f32_e32 v19, v19
	v_pk_mul_f32 v[12:13], v[160:161], v[128:129]
	v_pk_add_f32 v[14:15], v[14:15], 1.0 op_sel_hi:[1,0]
	v_mov_b32_e32 v3, v1
	v_pk_mul_f32 v[16:17], v[18:19], v[16:17]
	v_exp_f32_e64 v18, -v162
	v_exp_f32_e64 v19, -v163
	v_rcp_f32_e32 v14, v14
	v_rcp_f32_e32 v15, v15
	v_mov_b32_e32 v2, v189
	v_pk_add_f32 v[18:19], v[18:19], 1.0 op_sel_hi:[1,0]
	s_lshl_b32 s22, s52, 7
	v_rcp_f32_e32 v18, v18
	v_rcp_f32_e32 v19, v19
	v_pk_mul_f32 v[12:13], v[14:15], v[12:13]
	v_pk_mul_f32 v[14:15], v[158:159], v[126:127]
	v_med3_f32 v7, v12, s13, v250
	v_pk_mul_f32 v[10:11], v[18:19], v[10:11]
	v_exp_f32_e64 v18, -v158
	v_exp_f32_e64 v19, -v159
	v_med3_f32 v12, v13, s13, v250
	v_med3_f32 v13, v10, s13, v250
	v_mov_b32_e32 v10, v35
	v_pk_add_f32 v[18:19], v[18:19], 1.0 op_sel_hi:[1,0]
	v_cvt_pk_fp8_f32 v10, v7, v12
	v_rcp_f32_e32 v18, v18
	v_rcp_f32_e32 v19, v19
	v_med3_f32 v11, v11, s13, v250
	v_cvt_pk_fp8_f32 v10, v13, v11 op_sel:[0,0,1]
	v_med3_f32 v7, v16, s13, v250
	v_pk_mul_f32 v[14:15], v[18:19], v[14:15]
	v_exp_f32_e64 v18, -v148
	v_exp_f32_e64 v19, -v149
	v_med3_f32 v12, v17, s13, v250
	v_mov_b32_e32 v11, v35
	v_pk_mul_f32 v[16:17], v[148:149], v[116:117]
	v_pk_add_f32 v[18:19], v[18:19], 1.0 op_sel_hi:[1,0]
	v_cvt_pk_fp8_f32 v11, v7, v12
	v_rcp_f32_e32 v18, v18
	v_rcp_f32_e32 v19, v19
	s_or_b32 s22, s22, s46
	v_pk_mul_f32 v[16:17], v[18:19], v[16:17]
	v_exp_f32_e64 v18, -v154
	v_exp_f32_e64 v19, -v155
	s_lshl_b32 s14, s53, 8
	v_lshl_add_u32 v2, v2, 3, s22
	v_readlane_b32 s22, v254, 4
	v_med3_f32 v13, v14, s13, v250
	v_med3_f32 v14, v15, s13, v250
	s_add_i32 s14, s14, s45
	v_readlane_b32 s23, v254, 5
	v_cvt_pk_fp8_f32 v11, v13, v14 op_sel:[0,0,1]
	v_pk_add_f32 v[18:19], v[18:19], 1.0 op_sel_hi:[1,0]
	v_add_u32_e32 v6, s14, v3
	v_mov_b64_e32 v[4:5], s[22:23]
	s_movk_i32 s14, 0xb00
	v_rcp_f32_e32 v18, v18
	v_rcp_f32_e32 v19, v19
	v_ashrrev_i32_e32 v3, 31, v2
	v_mad_i64_i32 v[8:9], s[22:23], v6, s14, v[4:5]
	v_lshl_add_u64 v[8:9], v[8:9], 0, v[2:3]
	global_store_dwordx2 v[8:9], v[10:11], off
	v_pk_mul_f32 v[10:11], v[154:155], v[122:123]
	v_exp_f32_e64 v14, -v152
	v_exp_f32_e64 v15, -v153
	v_pk_mul_f32 v[10:11], v[18:19], v[10:11]
	v_exp_f32_e64 v18, -v150
	v_exp_f32_e64 v19, -v151
	v_pk_add_f32 v[14:15], v[14:15], 1.0 op_sel_hi:[1,0]
	v_pk_mul_f32 v[12:13], v[152:153], v[120:121]
	v_rcp_f32_e32 v14, v14
	v_rcp_f32_e32 v15, v15
	v_pk_add_f32 v[18:19], v[18:19], 1.0 op_sel_hi:[1,0]
	v_add_u32_e32 v7, 16, v6
	v_rcp_f32_e32 v18, v18
	v_rcp_f32_e32 v19, v19
	v_pk_mul_f32 v[12:13], v[14:15], v[12:13]
	v_pk_mul_f32 v[14:15], v[150:151], v[118:119]
	v_mad_i64_i32 v[8:9], s[22:23], v7, s14, v[4:5]
	v_pk_mul_f32 v[14:15], v[18:19], v[14:15]
	v_exp_f32_e64 v18, -v140
	v_exp_f32_e64 v19, -v141
	v_med3_f32 v7, v12, s13, v250
	v_med3_f32 v12, v13, s13, v250
	v_med3_f32 v13, v10, s13, v250
	v_mov_b32_e32 v10, v35
	v_cvt_pk_fp8_f32 v10, v7, v12
	v_pk_add_f32 v[18:19], v[18:19], 1.0 op_sel_hi:[1,0]
	v_med3_f32 v11, v11, s13, v250
	v_rcp_f32_e32 v18, v18
	v_rcp_f32_e32 v19, v19
	v_cvt_pk_fp8_f32 v10, v13, v11 op_sel:[0,0,1]
	v_med3_f32 v7, v16, s13, v250
	v_med3_f32 v12, v17, s13, v250
	v_mov_b32_e32 v11, v35
	v_pk_mul_f32 v[16:17], v[140:141], v[108:109]
	v_cvt_pk_fp8_f32 v11, v7, v12
	v_pk_mul_f32 v[16:17], v[18:19], v[16:17]
	v_exp_f32_e64 v18, -v146
	v_exp_f32_e64 v19, -v147
	v_med3_f32 v13, v14, s13, v250
	v_med3_f32 v14, v15, s13, v250
	v_cvt_pk_fp8_f32 v11, v13, v14 op_sel:[0,0,1]
	v_pk_add_f32 v[18:19], v[18:19], 1.0 op_sel_hi:[1,0]
	v_lshl_add_u64 v[8:9], v[8:9], 0, v[2:3]
	v_rcp_f32_e32 v18, v18
	v_rcp_f32_e32 v19, v19
	global_store_dwordx2 v[8:9], v[10:11], off
	s_and_b64 vcc, exec, s[8:9]
	s_cbranch_vccz .Lepi_nobar_2
	s_barrier
.Lepi_nobar_2:
	v_pk_mul_f32 v[10:11], v[146:147], v[114:115]
	v_exp_f32_e64 v14, -v144
	v_exp_f32_e64 v15, -v145
	v_pk_mul_f32 v[10:11], v[18:19], v[10:11]
	v_exp_f32_e64 v18, -v142
	v_exp_f32_e64 v19, -v143
	v_pk_add_f32 v[14:15], v[14:15], 1.0 op_sel_hi:[1,0]
	v_pk_mul_f32 v[12:13], v[144:145], v[112:113]
	v_rcp_f32_e32 v14, v14
	v_rcp_f32_e32 v15, v15
	v_pk_add_f32 v[18:19], v[18:19], 1.0 op_sel_hi:[1,0]
	v_add_u32_e32 v7, 32, v6
	v_rcp_f32_e32 v18, v18
	v_rcp_f32_e32 v19, v19
	v_pk_mul_f32 v[12:13], v[14:15], v[12:13]
	v_pk_mul_f32 v[14:15], v[142:143], v[110:111]
	v_mad_i64_i32 v[8:9], s[22:23], v7, s14, v[4:5]
	v_pk_mul_f32 v[14:15], v[18:19], v[14:15]
	v_exp_f32_e64 v18, -v132
	v_exp_f32_e64 v19, -v133
	v_med3_f32 v7, v12, s13, v250
	v_med3_f32 v12, v13, s13, v250
	v_med3_f32 v13, v10, s13, v250
	v_mov_b32_e32 v10, v35
	v_cvt_pk_fp8_f32 v10, v7, v12
	v_pk_add_f32 v[18:19], v[18:19], 1.0 op_sel_hi:[1,0]
	v_med3_f32 v11, v11, s13, v250
	v_rcp_f32_e32 v18, v18
	v_rcp_f32_e32 v19, v19
	v_cvt_pk_fp8_f32 v10, v13, v11 op_sel:[0,0,1]
	v_med3_f32 v7, v16, s13, v250
	v_med3_f32 v12, v17, s13, v250
	v_mov_b32_e32 v11, v35
	v_pk_mul_f32 v[16:17], v[132:133], v[100:101]
	v_cvt_pk_fp8_f32 v11, v7, v12
	v_pk_mul_f32 v[16:17], v[18:19], v[16:17]
	v_exp_f32_e64 v18, -v138
	v_exp_f32_e64 v19, -v139
	v_med3_f32 v13, v14, s13, v250
	v_med3_f32 v14, v15, s13, v250
	v_cvt_pk_fp8_f32 v11, v13, v14 op_sel:[0,0,1]
	v_pk_add_f32 v[18:19], v[18:19], 1.0 op_sel_hi:[1,0]
	v_lshl_add_u64 v[8:9], v[8:9], 0, v[2:3]
	v_rcp_f32_e32 v18, v18
	v_rcp_f32_e32 v19, v19
	global_store_dwordx2 v[8:9], v[10:11], off
	v_pk_mul_f32 v[10:11], v[138:139], v[106:107]
	v_exp_f32_e64 v14, -v136
	v_exp_f32_e64 v15, -v137
	v_pk_mul_f32 v[10:11], v[18:19], v[10:11]
	v_exp_f32_e64 v18, -v134
	v_exp_f32_e64 v19, -v135
	v_pk_add_f32 v[14:15], v[14:15], 1.0 op_sel_hi:[1,0]
	v_pk_mul_f32 v[12:13], v[136:137], v[104:105]
	v_rcp_f32_e32 v14, v14
	v_rcp_f32_e32 v15, v15
	v_pk_add_f32 v[18:19], v[18:19], 1.0 op_sel_hi:[1,0]
	v_add_u32_e32 v7, 48, v6
	v_rcp_f32_e32 v18, v18
	v_rcp_f32_e32 v19, v19
	v_pk_mul_f32 v[12:13], v[14:15], v[12:13]
	v_pk_mul_f32 v[14:15], v[134:135], v[102:103]
	v_mad_i64_i32 v[8:9], s[22:23], v7, s14, v[4:5]
	v_pk_mul_f32 v[14:15], v[18:19], v[14:15]
	v_exp_f32_e64 v18, -v92
	v_exp_f32_e64 v19, -v93
	v_med3_f32 v7, v12, s13, v250
	v_med3_f32 v12, v13, s13, v250
	v_med3_f32 v13, v10, s13, v250
	v_mov_b32_e32 v10, v35
	v_cvt_pk_fp8_f32 v10, v7, v12
	v_pk_add_f32 v[18:19], v[18:19], 1.0 op_sel_hi:[1,0]
	v_med3_f32 v11, v11, s13, v250
	v_rcp_f32_e32 v18, v18
	v_rcp_f32_e32 v19, v19
	v_cvt_pk_fp8_f32 v10, v13, v11 op_sel:[0,0,1]
	v_med3_f32 v7, v16, s13, v250
	v_med3_f32 v12, v17, s13, v250
	v_mov_b32_e32 v11, v35
	v_pk_mul_f32 v[16:17], v[92:93], v[60:61]
	v_cvt_pk_fp8_f32 v11, v7, v12
	v_pk_mul_f32 v[16:17], v[18:19], v[16:17]
	v_exp_f32_e64 v18, -v98
	v_exp_f32_e64 v19, -v99
	v_med3_f32 v13, v14, s13, v250
	v_med3_f32 v14, v15, s13, v250
	v_cvt_pk_fp8_f32 v11, v13, v14 op_sel:[0,0,1]
	v_pk_add_f32 v[18:19], v[18:19], 1.0 op_sel_hi:[1,0]
	v_lshl_add_u64 v[8:9], v[8:9], 0, v[2:3]
	v_rcp_f32_e32 v18, v18
	v_rcp_f32_e32 v19, v19
	global_store_dwordx2 v[8:9], v[10:11], off
	v_pk_mul_f32 v[10:11], v[98:99], v[66:67]
	v_exp_f32_e64 v14, -v96
	v_exp_f32_e64 v15, -v97
	v_pk_mul_f32 v[10:11], v[18:19], v[10:11]
	v_exp_f32_e64 v18, -v94
	v_exp_f32_e64 v19, -v95
	v_pk_add_f32 v[14:15], v[14:15], 1.0 op_sel_hi:[1,0]
	v_pk_mul_f32 v[12:13], v[96:97], v[64:65]
	v_rcp_f32_e32 v14, v14
	v_rcp_f32_e32 v15, v15
	v_pk_add_f32 v[18:19], v[18:19], 1.0 op_sel_hi:[1,0]
	v_add_u32_e32 v7, 0x80, v6
	v_rcp_f32_e32 v18, v18
	v_rcp_f32_e32 v19, v19
	v_pk_mul_f32 v[12:13], v[14:15], v[12:13]
	v_pk_mul_f32 v[14:15], v[94:95], v[62:63]
	v_mad_i64_i32 v[8:9], s[22:23], v7, s14, v[4:5]
	v_pk_mul_f32 v[14:15], v[18:19], v[14:15]
	v_exp_f32_e64 v18, -v84
	v_exp_f32_e64 v19, -v85
	v_med3_f32 v7, v12, s13, v250
	v_med3_f32 v12, v13, s13, v250
	v_med3_f32 v13, v10, s13, v250
	v_mov_b32_e32 v10, v35
	v_cvt_pk_fp8_f32 v10, v7, v12
	v_pk_add_f32 v[18:19], v[18:19], 1.0 op_sel_hi:[1,0]
	v_med3_f32 v11, v11, s13, v250
	v_rcp_f32_e32 v18, v18
	v_rcp_f32_e32 v19, v19
	v_cvt_pk_fp8_f32 v10, v13, v11 op_sel:[0,0,1]
	v_med3_f32 v7, v16, s13, v250
	v_med3_f32 v12, v17, s13, v250
	v_mov_b32_e32 v11, v35
	v_pk_mul_f32 v[16:17], v[84:85], v[52:53]
	v_cvt_pk_fp8_f32 v11, v7, v12
	v_pk_mul_f32 v[16:17], v[18:19], v[16:17]
	v_exp_f32_e64 v18, -v90
	v_exp_f32_e64 v19, -v91
	v_med3_f32 v13, v14, s13, v250
	v_med3_f32 v14, v15, s13, v250
	v_cvt_pk_fp8_f32 v11, v13, v14 op_sel:[0,0,1]
	v_pk_add_f32 v[18:19], v[18:19], 1.0 op_sel_hi:[1,0]
	v_lshl_add_u64 v[8:9], v[8:9], 0, v[2:3]
	v_rcp_f32_e32 v18, v18
	v_rcp_f32_e32 v19, v19
	v_exp_f32_e64 v14, -v88
	v_exp_f32_e64 v15, -v89
	global_store_dwordx2 v[8:9], v[10:11], off
	v_pk_mul_f32 v[10:11], v[90:91], v[58:59]
	v_pk_mul_f32 v[12:13], v[88:89], v[56:57]
	v_pk_mul_f32 v[10:11], v[18:19], v[10:11]
	v_exp_f32_e64 v18, -v86
	v_exp_f32_e64 v19, -v87
	v_pk_add_f32 v[14:15], v[14:15], 1.0 op_sel_hi:[1,0]
	v_add_u32_e32 v7, 0x90, v6
	v_rcp_f32_e32 v14, v14
	v_rcp_f32_e32 v15, v15
	v_pk_add_f32 v[18:19], v[18:19], 1.0 op_sel_hi:[1,0]
	v_mad_i64_i32 v[8:9], s[22:23], v7, s14, v[4:5]
	v_rcp_f32_e32 v18, v18
	v_rcp_f32_e32 v19, v19
	v_pk_mul_f32 v[12:13], v[14:15], v[12:13]
	v_pk_mul_f32 v[14:15], v[86:87], v[54:55]
	v_med3_f32 v7, v12, s13, v250
	v_med3_f32 v12, v13, s13, v250
	v_med3_f32 v13, v10, s13, v250
	v_mov_b32_e32 v10, v35
	v_pk_mul_f32 v[14:15], v[18:19], v[14:15]
	v_cvt_pk_fp8_f32 v10, v7, v12
	v_exp_f32_e64 v18, -v76
	v_exp_f32_e64 v19, -v77
	v_med3_f32 v11, v11, s13, v250
	v_cvt_pk_fp8_f32 v10, v13, v11 op_sel:[0,0,1]
	v_med3_f32 v7, v16, s13, v250
	v_med3_f32 v12, v17, s13, v250
	v_mov_b32_e32 v11, v35
	v_pk_add_f32 v[18:19], v[18:19], 1.0 op_sel_hi:[1,0]
	v_cvt_pk_fp8_f32 v11, v7, v12
	v_rcp_f32_e32 v18, v18
	v_rcp_f32_e32 v19, v19
	v_med3_f32 v13, v14, s13, v250
	v_med3_f32 v14, v15, s13, v250
	v_pk_mul_f32 v[16:17], v[76:77], v[44:45]
	v_cvt_pk_fp8_f32 v11, v13, v14 op_sel:[0,0,1]
	v_exp_f32_e64 v14, -v80
	v_exp_f32_e64 v15, -v81
	v_pk_mul_f32 v[16:17], v[18:19], v[16:17]
	v_exp_f32_e64 v18, -v82
	v_exp_f32_e64 v19, -v83
	v_pk_add_f32 v[14:15], v[14:15], 1.0 op_sel_hi:[1,0]
	v_lshl_add_u64 v[8:9], v[8:9], 0, v[2:3]
	v_rcp_f32_e32 v14, v14
	v_pk_add_f32 v[18:19], v[18:19], 1.0 op_sel_hi:[1,0]
	v_rcp_f32_e32 v15, v15
	v_rcp_f32_e32 v18, v18
	v_rcp_f32_e32 v19, v19
	global_store_dwordx2 v[8:9], v[10:11], off
	v_pk_mul_f32 v[10:11], v[82:83], v[50:51]
	v_pk_mul_f32 v[12:13], v[80:81], v[48:49]
	v_add_u32_e32 v7, 0xa0, v6
	v_pk_mul_f32 v[12:13], v[14:15], v[12:13]
	v_pk_mul_f32 v[10:11], v[18:19], v[10:11]
	v_exp_f32_e64 v18, -v78
	v_exp_f32_e64 v19, -v79
	v_mad_i64_i32 v[8:9], s[22:23], v7, s14, v[4:5]
	v_med3_f32 v7, v12, s13, v250
	v_med3_f32 v12, v13, s13, v250
	v_med3_f32 v13, v10, s13, v250
	v_mov_b32_e32 v10, v35
	v_cvt_pk_fp8_f32 v10, v7, v12
	v_pk_add_f32 v[18:19], v[18:19], 1.0 op_sel_hi:[1,0]
	v_med3_f32 v11, v11, s13, v250
	v_rcp_f32_e32 v18, v18
	v_rcp_f32_e32 v19, v19
	v_cvt_pk_fp8_f32 v10, v13, v11 op_sel:[0,0,1]
	v_med3_f32 v7, v16, s13, v250
	v_med3_f32 v12, v17, s13, v250
	v_mov_b32_e32 v11, v35
	v_cvt_pk_fp8_f32 v11, v7, v12
	v_pk_mul_f32 v[14:15], v[78:79], v[46:47]
	v_lshl_add_u64 v[8:9], v[8:9], 0, v[2:3]
	v_pk_mul_f32 v[14:15], v[18:19], v[14:15]
	v_add_u32_e32 v6, 0xb0, v6
	v_med3_f32 v13, v14, s13, v250
	v_med3_f32 v14, v15, s13, v250
	v_cvt_pk_fp8_f32 v11, v13, v14 op_sel:[0,0,1]
	v_exp_f32_e64 v14, -v68
	v_exp_f32_e64 v15, -v69
	v_pk_mul_f32 v[12:13], v[68:69], v[36:37]
	global_store_dwordx2 v[8:9], v[10:11], off
	v_exp_f32_e64 v10, -v72
	v_pk_add_f32 v[14:15], v[14:15], 1.0 op_sel_hi:[1,0]
	v_exp_f32_e64 v11, -v73
	v_rcp_f32_e32 v14, v14
	v_rcp_f32_e32 v15, v15
	v_mad_i64_i32 v[4:5], s[22:23], v6, s14, v[4:5]
	v_pk_add_f32 v[10:11], v[10:11], 1.0 op_sel_hi:[1,0]
	v_pk_mul_f32 v[12:13], v[14:15], v[12:13]
	v_exp_f32_e64 v14, -v74
	v_exp_f32_e64 v15, -v75
	v_rcp_f32_e32 v10, v10
	v_rcp_f32_e32 v11, v11
	v_pk_mul_f32 v[6:7], v[74:75], v[42:43]
	v_pk_add_f32 v[14:15], v[14:15], 1.0 op_sel_hi:[1,0]
	v_pk_mul_f32 v[8:9], v[72:73], v[40:41]
	v_rcp_f32_e32 v14, v14
	v_rcp_f32_e32 v15, v15
	v_pk_mul_f32 v[8:9], v[10:11], v[8:9]
	v_lshl_add_u64 v[2:3], v[4:5], 0, v[2:3]
	v_med3_f32 v5, v8, s13, v250
	v_pk_mul_f32 v[6:7], v[14:15], v[6:7]
	v_exp_f32_e64 v14, -v70
	v_exp_f32_e64 v15, -v71
	v_med3_f32 v8, v9, s13, v250
	v_mov_b32_e32 v4, v35
	v_cvt_pk_fp8_f32 v4, v5, v8
	v_pk_add_f32 v[14:15], v[14:15], 1.0 op_sel_hi:[1,0]
	v_med3_f32 v6, v6, s13, v250
	v_rcp_f32_e32 v14, v14
	v_rcp_f32_e32 v15, v15
	v_med3_f32 v7, v7, s13, v250
	v_cvt_pk_fp8_f32 v4, v6, v7 op_sel:[0,0,1]
	v_med3_f32 v6, v12, s13, v250
	v_med3_f32 v7, v13, s13, v250
	v_mov_b32_e32 v5, v35
	v_cvt_pk_fp8_f32 v5, v6, v7
	v_pk_mul_f32 v[10:11], v[70:71], v[38:39]
	s_mov_b64 s[22:23], -1
	v_pk_mul_f32 v[10:11], v[14:15], v[10:11]
	s_andn2_b64 vcc, exec, s[4:5]
	v_med3_f32 v8, v10, s13, v250
	v_med3_f32 v9, v11, s13, v250
	v_cvt_pk_fp8_f32 v5, v8, v9 op_sel:[0,0,1]
	s_mov_b32 s58, 0x19b00000
	v_readlane_b32 s59, v255, 10
	s_mov_b32 s60, 0xff61b1e6
	s_mov_b32 s56, 0x3a800000
	s_mov_b64 s[62:63], 0x800
	s_mov_b32 s64, 0x3b000000
	global_store_dwordx2 v[2:3], v[4:5], off
	s_cbranch_vccnz .LBB0_1083
	s_andn2_b64 vcc, exec, s[6:7]
	s_cbranch_vccnz .LBB0_1082
	s_barrier
	s_branch .LBB0_1082
